# stack3
# speedup vs baseline: 1.0077x; 1.0034x over previous
_Z5k_fc2PKfS0_S0_S0_Pf:
	s_load_dwordx8 s[4:11], s[0:1], 0x0
	v_lshlrev_b32_e32 v2, 2, v0
	s_ashr_i32 s3, s2, 31
	v_mov_b32_e32 v3, 0
	s_waitcnt lgkmcnt(0)
	global_load_dword v1, v2, s[6:7]
	s_load_dwordx2 s[6:7], s[0:1], 0x20
	s_lshl_b64 s[0:1], s[2:3], 11
	s_add_u32 s0, s4, s0
	s_addc_u32 s1, s5, s1
	v_lshl_add_u64 v[2:3], s[0:1], 0, v[2:3]
	s_mov_b64 s[0:1], 0
	s_lshl_b64 s[0:1], s[2:3], 11
	s_add_u32 s0, s4, s0
	s_addc_u32 s1, s5, s1
	v_lshlrev_b32_e32 v4, 2, v0
	global_load_dword v32, v4, s[0:1]
	s_add_u32 s0, s0, 0x20000
	s_addc_u32 s1, s1, 0
	global_load_dword v33, v4, s[0:1]
	s_add_u32 s0, s0, 0x20000
	s_addc_u32 s1, s1, 0
	global_load_dword v34, v4, s[0:1]
	s_add_u32 s0, s0, 0x20000
	s_addc_u32 s1, s1, 0
	global_load_dword v35, v4, s[0:1]
	s_add_u32 s0, s0, 0x20000
	s_addc_u32 s1, s1, 0
	global_load_dword v36, v4, s[0:1]
	s_add_u32 s0, s0, 0x20000
	s_addc_u32 s1, s1, 0
	global_load_dword v37, v4, s[0:1]
	s_add_u32 s0, s0, 0x20000
	s_addc_u32 s1, s1, 0
	global_load_dword v38, v4, s[0:1]
	s_add_u32 s0, s0, 0x20000
	s_addc_u32 s1, s1, 0
	global_load_dword v39, v4, s[0:1]
	s_add_u32 s0, s0, 0x20000
	s_addc_u32 s1, s1, 0
	global_load_dword v40, v4, s[0:1]
	s_add_u32 s0, s0, 0x20000
	s_addc_u32 s1, s1, 0
	global_load_dword v41, v4, s[0:1]
	s_add_u32 s0, s0, 0x20000
	s_addc_u32 s1, s1, 0
	global_load_dword v42, v4, s[0:1]
	s_add_u32 s0, s0, 0x20000
	s_addc_u32 s1, s1, 0
	global_load_dword v43, v4, s[0:1]
	s_add_u32 s0, s0, 0x20000
	s_addc_u32 s1, s1, 0
	global_load_dword v44, v4, s[0:1]
	s_add_u32 s0, s0, 0x20000
	s_addc_u32 s1, s1, 0
	global_load_dword v45, v4, s[0:1]
	s_add_u32 s0, s0, 0x20000
	s_addc_u32 s1, s1, 0
	global_load_dword v46, v4, s[0:1]
	s_add_u32 s0, s0, 0x20000
	s_addc_u32 s1, s1, 0
	global_load_dword v47, v4, s[0:1]
	s_add_u32 s0, s0, 0x20000
	s_addc_u32 s1, s1, 0
	global_load_dword v48, v4, s[0:1]
	s_add_u32 s0, s0, 0x20000
	s_addc_u32 s1, s1, 0
	global_load_dword v49, v4, s[0:1]
	s_add_u32 s0, s0, 0x20000
	s_addc_u32 s1, s1, 0
	global_load_dword v50, v4, s[0:1]
	s_add_u32 s0, s0, 0x20000
	s_addc_u32 s1, s1, 0
	global_load_dword v51, v4, s[0:1]
	s_add_u32 s0, s0, 0x20000
	s_addc_u32 s1, s1, 0
	global_load_dword v52, v4, s[0:1]
	s_add_u32 s0, s0, 0x20000
	s_addc_u32 s1, s1, 0
	global_load_dword v53, v4, s[0:1]
	s_add_u32 s0, s0, 0x20000
	s_addc_u32 s1, s1, 0
	global_load_dword v54, v4, s[0:1]
	s_add_u32 s0, s0, 0x20000
	s_addc_u32 s1, s1, 0
	global_load_dword v55, v4, s[0:1]
	s_add_u32 s0, s0, 0x20000
	s_addc_u32 s1, s1, 0
	global_load_dword v56, v4, s[0:1]
	s_add_u32 s0, s0, 0x20000
	s_addc_u32 s1, s1, 0
	global_load_dword v57, v4, s[0:1]
	s_add_u32 s0, s0, 0x20000
	s_addc_u32 s1, s1, 0
	global_load_dword v58, v4, s[0:1]
	s_add_u32 s0, s0, 0x20000
	s_addc_u32 s1, s1, 0
	global_load_dword v59, v4, s[0:1]
	s_add_u32 s0, s0, 0x20000
	s_addc_u32 s1, s1, 0
	global_load_dword v60, v4, s[0:1]
	s_add_u32 s0, s0, 0x20000
	s_addc_u32 s1, s1, 0
	global_load_dword v61, v4, s[0:1]
	s_add_u32 s0, s0, 0x20000
	s_addc_u32 s1, s1, 0
	global_load_dword v62, v4, s[0:1]
	s_add_u32 s0, s0, 0x20000
	s_addc_u32 s1, s1, 0
	global_load_dword v63, v4, s[0:1]
	s_add_u32 s0, s0, 0x20000
	s_addc_u32 s1, s1, 0
	global_load_dword v64, v4, s[0:1]
	s_add_u32 s0, s0, 0x20000
	s_addc_u32 s1, s1, 0
	global_load_dword v65, v4, s[0:1]
	s_add_u32 s0, s0, 0x20000
	s_addc_u32 s1, s1, 0
	global_load_dword v66, v4, s[0:1]
	s_add_u32 s0, s0, 0x20000
	s_addc_u32 s1, s1, 0
	global_load_dword v67, v4, s[0:1]
	s_add_u32 s0, s0, 0x20000
	s_addc_u32 s1, s1, 0
	global_load_dword v68, v4, s[0:1]
	s_add_u32 s0, s0, 0x20000
	s_addc_u32 s1, s1, 0
	global_load_dword v69, v4, s[0:1]
	s_add_u32 s0, s0, 0x20000
	s_addc_u32 s1, s1, 0
	global_load_dword v70, v4, s[0:1]
	s_add_u32 s0, s0, 0x20000
	s_addc_u32 s1, s1, 0
	global_load_dword v71, v4, s[0:1]
	s_add_u32 s0, s0, 0x20000
	s_addc_u32 s1, s1, 0
	global_load_dword v72, v4, s[0:1]
	s_add_u32 s0, s0, 0x20000
	s_addc_u32 s1, s1, 0
	global_load_dword v73, v4, s[0:1]
	s_add_u32 s0, s0, 0x20000
	s_addc_u32 s1, s1, 0
	global_load_dword v74, v4, s[0:1]
	s_add_u32 s0, s0, 0x20000
	s_addc_u32 s1, s1, 0
	global_load_dword v75, v4, s[0:1]
	s_add_u32 s0, s0, 0x20000
	s_addc_u32 s1, s1, 0
	global_load_dword v76, v4, s[0:1]
	s_add_u32 s0, s0, 0x20000
	s_addc_u32 s1, s1, 0
	global_load_dword v77, v4, s[0:1]
	s_add_u32 s0, s0, 0x20000
	s_addc_u32 s1, s1, 0
	global_load_dword v78, v4, s[0:1]
	s_add_u32 s0, s0, 0x20000
	s_addc_u32 s1, s1, 0
	global_load_dword v79, v4, s[0:1]
	s_add_u32 s0, s0, 0x20000
	s_addc_u32 s1, s1, 0
	global_load_dword v80, v4, s[0:1]
	s_add_u32 s0, s0, 0x20000
	s_addc_u32 s1, s1, 0
	global_load_dword v81, v4, s[0:1]
	s_add_u32 s0, s0, 0x20000
	s_addc_u32 s1, s1, 0
	global_load_dword v82, v4, s[0:1]
	s_add_u32 s0, s0, 0x20000
	s_addc_u32 s1, s1, 0
	global_load_dword v83, v4, s[0:1]
	s_add_u32 s0, s0, 0x20000
	s_addc_u32 s1, s1, 0
	global_load_dword v84, v4, s[0:1]
	s_add_u32 s0, s0, 0x20000
	s_addc_u32 s1, s1, 0
	global_load_dword v85, v4, s[0:1]
	s_add_u32 s0, s0, 0x20000
	s_addc_u32 s1, s1, 0
	global_load_dword v86, v4, s[0:1]
	s_add_u32 s0, s0, 0x20000
	s_addc_u32 s1, s1, 0
	global_load_dword v87, v4, s[0:1]
	s_add_u32 s0, s0, 0x20000
	s_addc_u32 s1, s1, 0
	global_load_dword v88, v4, s[0:1]
	s_add_u32 s0, s0, 0x20000
	s_addc_u32 s1, s1, 0
	global_load_dword v89, v4, s[0:1]
	s_add_u32 s0, s0, 0x20000
	s_addc_u32 s1, s1, 0
	global_load_dword v90, v4, s[0:1]
	s_add_u32 s0, s0, 0x20000
	s_addc_u32 s1, s1, 0
	global_load_dword v91, v4, s[0:1]
	s_add_u32 s0, s0, 0x20000
	s_addc_u32 s1, s1, 0
	global_load_dword v92, v4, s[0:1]
	s_add_u32 s0, s0, 0x20000
	s_addc_u32 s1, s1, 0
	global_load_dword v93, v4, s[0:1]
	s_add_u32 s0, s0, 0x20000
	s_addc_u32 s1, s1, 0
	global_load_dword v94, v4, s[0:1]
	s_add_u32 s0, s0, 0x20000
	s_addc_u32 s1, s1, 0
	global_load_dword v95, v4, s[0:1]
	s_add_u32 s0, s0, 0x20000
	s_addc_u32 s1, s1, 0
	s_waitcnt vmcnt(63)
	v_add_f32_e32 v1, v1, v32
	global_load_dword v32, v4, s[0:1]
	s_add_u32 s0, s0, 0x20000
	s_addc_u32 s1, s1, 0
	s_waitcnt vmcnt(63)
	v_add_f32_e32 v1, v1, v33
	global_load_dword v33, v4, s[0:1]
	s_add_u32 s0, s0, 0x20000
	s_addc_u32 s1, s1, 0
	s_waitcnt vmcnt(63)
	v_add_f32_e32 v1, v1, v34
	global_load_dword v34, v4, s[0:1]
	s_add_u32 s0, s0, 0x20000
	s_addc_u32 s1, s1, 0
	s_waitcnt vmcnt(63)
	v_add_f32_e32 v1, v1, v35
	global_load_dword v35, v4, s[0:1]
	s_add_u32 s0, s0, 0x20000
	s_addc_u32 s1, s1, 0
	s_waitcnt vmcnt(63)
	v_add_f32_e32 v1, v1, v36
	global_load_dword v36, v4, s[0:1]
	s_add_u32 s0, s0, 0x20000
	s_addc_u32 s1, s1, 0
	s_waitcnt vmcnt(63)
	v_add_f32_e32 v1, v1, v37
	global_load_dword v37, v4, s[0:1]
	s_add_u32 s0, s0, 0x20000
	s_addc_u32 s1, s1, 0
	s_waitcnt vmcnt(63)
	v_add_f32_e32 v1, v1, v38
	global_load_dword v38, v4, s[0:1]
	s_add_u32 s0, s0, 0x20000
	s_addc_u32 s1, s1, 0
	s_waitcnt vmcnt(63)
	v_add_f32_e32 v1, v1, v39
	global_load_dword v39, v4, s[0:1]
	s_add_u32 s0, s0, 0x20000
	s_addc_u32 s1, s1, 0
	s_waitcnt vmcnt(63)
	v_add_f32_e32 v1, v1, v40
	global_load_dword v40, v4, s[0:1]
	s_add_u32 s0, s0, 0x20000
	s_addc_u32 s1, s1, 0
	s_waitcnt vmcnt(63)
	v_add_f32_e32 v1, v1, v41
	global_load_dword v41, v4, s[0:1]
	s_add_u32 s0, s0, 0x20000
	s_addc_u32 s1, s1, 0
	s_waitcnt vmcnt(63)
	v_add_f32_e32 v1, v1, v42
	global_load_dword v42, v4, s[0:1]
	s_add_u32 s0, s0, 0x20000
	s_addc_u32 s1, s1, 0
	s_waitcnt vmcnt(63)
	v_add_f32_e32 v1, v1, v43
	global_load_dword v43, v4, s[0:1]
	s_add_u32 s0, s0, 0x20000
	s_addc_u32 s1, s1, 0
	s_waitcnt vmcnt(63)
	v_add_f32_e32 v1, v1, v44
	global_load_dword v44, v4, s[0:1]
	s_add_u32 s0, s0, 0x20000
	s_addc_u32 s1, s1, 0
	s_waitcnt vmcnt(63)
	v_add_f32_e32 v1, v1, v45
	global_load_dword v45, v4, s[0:1]
	s_add_u32 s0, s0, 0x20000
	s_addc_u32 s1, s1, 0
	s_waitcnt vmcnt(63)
	v_add_f32_e32 v1, v1, v46
	global_load_dword v46, v4, s[0:1]
	s_add_u32 s0, s0, 0x20000
	s_addc_u32 s1, s1, 0
	s_waitcnt vmcnt(63)
	v_add_f32_e32 v1, v1, v47
	global_load_dword v47, v4, s[0:1]
	s_add_u32 s0, s0, 0x20000
	s_addc_u32 s1, s1, 0
	s_waitcnt vmcnt(63)
	v_add_f32_e32 v1, v1, v48
	global_load_dword v48, v4, s[0:1]
	s_add_u32 s0, s0, 0x20000
	s_addc_u32 s1, s1, 0
	s_waitcnt vmcnt(63)
	v_add_f32_e32 v1, v1, v49
	global_load_dword v49, v4, s[0:1]
	s_add_u32 s0, s0, 0x20000
	s_addc_u32 s1, s1, 0
	s_waitcnt vmcnt(63)
	v_add_f32_e32 v1, v1, v50
	global_load_dword v50, v4, s[0:1]
	s_add_u32 s0, s0, 0x20000
	s_addc_u32 s1, s1, 0
	s_waitcnt vmcnt(63)
	v_add_f32_e32 v1, v1, v51
	global_load_dword v51, v4, s[0:1]
	s_add_u32 s0, s0, 0x20000
	s_addc_u32 s1, s1, 0
	s_waitcnt vmcnt(63)
	v_add_f32_e32 v1, v1, v52
	global_load_dword v52, v4, s[0:1]
	s_add_u32 s0, s0, 0x20000
	s_addc_u32 s1, s1, 0
	s_waitcnt vmcnt(63)
	v_add_f32_e32 v1, v1, v53
	global_load_dword v53, v4, s[0:1]
	s_add_u32 s0, s0, 0x20000
	s_addc_u32 s1, s1, 0
	s_waitcnt vmcnt(63)
	v_add_f32_e32 v1, v1, v54
	global_load_dword v54, v4, s[0:1]
	s_add_u32 s0, s0, 0x20000
	s_addc_u32 s1, s1, 0
	s_waitcnt vmcnt(63)
	v_add_f32_e32 v1, v1, v55
	global_load_dword v55, v4, s[0:1]
	s_add_u32 s0, s0, 0x20000
	s_addc_u32 s1, s1, 0
	s_waitcnt vmcnt(63)
	v_add_f32_e32 v1, v1, v56
	global_load_dword v56, v4, s[0:1]
	s_add_u32 s0, s0, 0x20000
	s_addc_u32 s1, s1, 0
	s_waitcnt vmcnt(63)
	v_add_f32_e32 v1, v1, v57
	global_load_dword v57, v4, s[0:1]
	s_add_u32 s0, s0, 0x20000
	s_addc_u32 s1, s1, 0
	s_waitcnt vmcnt(63)
	v_add_f32_e32 v1, v1, v58
	global_load_dword v58, v4, s[0:1]
	s_add_u32 s0, s0, 0x20000
	s_addc_u32 s1, s1, 0
	s_waitcnt vmcnt(63)
	v_add_f32_e32 v1, v1, v59
	global_load_dword v59, v4, s[0:1]
	s_add_u32 s0, s0, 0x20000
	s_addc_u32 s1, s1, 0
	s_waitcnt vmcnt(63)
	v_add_f32_e32 v1, v1, v60
	global_load_dword v60, v4, s[0:1]
	s_add_u32 s0, s0, 0x20000
	s_addc_u32 s1, s1, 0
	s_waitcnt vmcnt(63)
	v_add_f32_e32 v1, v1, v61
	global_load_dword v61, v4, s[0:1]
	s_add_u32 s0, s0, 0x20000
	s_addc_u32 s1, s1, 0
	s_waitcnt vmcnt(63)
	v_add_f32_e32 v1, v1, v62
	global_load_dword v62, v4, s[0:1]
	s_add_u32 s0, s0, 0x20000
	s_addc_u32 s1, s1, 0
	s_waitcnt vmcnt(63)
	v_add_f32_e32 v1, v1, v63
	global_load_dword v63, v4, s[0:1]
	s_add_u32 s0, s0, 0x20000
	s_addc_u32 s1, s1, 0
	s_waitcnt vmcnt(63)
	v_add_f32_e32 v1, v1, v64
	global_load_dword v64, v4, s[0:1]
	s_add_u32 s0, s0, 0x20000
	s_addc_u32 s1, s1, 0
	s_waitcnt vmcnt(63)
	v_add_f32_e32 v1, v1, v65
	global_load_dword v65, v4, s[0:1]
	s_add_u32 s0, s0, 0x20000
	s_addc_u32 s1, s1, 0
	s_waitcnt vmcnt(63)
	v_add_f32_e32 v1, v1, v66
	global_load_dword v66, v4, s[0:1]
	s_add_u32 s0, s0, 0x20000
	s_addc_u32 s1, s1, 0
	s_waitcnt vmcnt(63)
	v_add_f32_e32 v1, v1, v67
	global_load_dword v67, v4, s[0:1]
	s_add_u32 s0, s0, 0x20000
	s_addc_u32 s1, s1, 0
	s_waitcnt vmcnt(63)
	v_add_f32_e32 v1, v1, v68
	global_load_dword v68, v4, s[0:1]
	s_add_u32 s0, s0, 0x20000
	s_addc_u32 s1, s1, 0
	s_waitcnt vmcnt(63)
	v_add_f32_e32 v1, v1, v69
	global_load_dword v69, v4, s[0:1]
	s_add_u32 s0, s0, 0x20000
	s_addc_u32 s1, s1, 0
	s_waitcnt vmcnt(63)
	v_add_f32_e32 v1, v1, v70
	global_load_dword v70, v4, s[0:1]
	s_add_u32 s0, s0, 0x20000
	s_addc_u32 s1, s1, 0
	s_waitcnt vmcnt(63)
	v_add_f32_e32 v1, v1, v71
	global_load_dword v71, v4, s[0:1]
	s_add_u32 s0, s0, 0x20000
	s_addc_u32 s1, s1, 0
	s_waitcnt vmcnt(63)
	v_add_f32_e32 v1, v1, v72
	global_load_dword v72, v4, s[0:1]
	s_add_u32 s0, s0, 0x20000
	s_addc_u32 s1, s1, 0
	s_waitcnt vmcnt(63)
	v_add_f32_e32 v1, v1, v73
	global_load_dword v73, v4, s[0:1]
	s_add_u32 s0, s0, 0x20000
	s_addc_u32 s1, s1, 0
	s_waitcnt vmcnt(63)
	v_add_f32_e32 v1, v1, v74
	global_load_dword v74, v4, s[0:1]
	s_add_u32 s0, s0, 0x20000
	s_addc_u32 s1, s1, 0
	s_waitcnt vmcnt(63)
	v_add_f32_e32 v1, v1, v75
	global_load_dword v75, v4, s[0:1]
	s_add_u32 s0, s0, 0x20000
	s_addc_u32 s1, s1, 0
	s_waitcnt vmcnt(63)
	v_add_f32_e32 v1, v1, v76
	global_load_dword v76, v4, s[0:1]
	s_add_u32 s0, s0, 0x20000
	s_addc_u32 s1, s1, 0
	s_waitcnt vmcnt(63)
	v_add_f32_e32 v1, v1, v77
	global_load_dword v77, v4, s[0:1]
	s_add_u32 s0, s0, 0x20000
	s_addc_u32 s1, s1, 0
	s_waitcnt vmcnt(63)
	v_add_f32_e32 v1, v1, v78
	global_load_dword v78, v4, s[0:1]
	s_add_u32 s0, s0, 0x20000
	s_addc_u32 s1, s1, 0
	s_waitcnt vmcnt(63)
	v_add_f32_e32 v1, v1, v79
	global_load_dword v79, v4, s[0:1]
	s_add_u32 s0, s0, 0x20000
	s_addc_u32 s1, s1, 0
	s_waitcnt vmcnt(63)
	v_add_f32_e32 v1, v1, v80
	global_load_dword v80, v4, s[0:1]
	s_add_u32 s0, s0, 0x20000
	s_addc_u32 s1, s1, 0
	s_waitcnt vmcnt(63)
	v_add_f32_e32 v1, v1, v81
	global_load_dword v81, v4, s[0:1]
	s_add_u32 s0, s0, 0x20000
	s_addc_u32 s1, s1, 0
	s_waitcnt vmcnt(63)
	v_add_f32_e32 v1, v1, v82
	global_load_dword v82, v4, s[0:1]
	s_add_u32 s0, s0, 0x20000
	s_addc_u32 s1, s1, 0
	s_waitcnt vmcnt(63)
	v_add_f32_e32 v1, v1, v83
	global_load_dword v83, v4, s[0:1]
	s_add_u32 s0, s0, 0x20000
	s_addc_u32 s1, s1, 0
	s_waitcnt vmcnt(63)
	v_add_f32_e32 v1, v1, v84
	global_load_dword v84, v4, s[0:1]
	s_add_u32 s0, s0, 0x20000
	s_addc_u32 s1, s1, 0
	s_waitcnt vmcnt(63)
	v_add_f32_e32 v1, v1, v85
	global_load_dword v85, v4, s[0:1]
	s_add_u32 s0, s0, 0x20000
	s_addc_u32 s1, s1, 0
	s_waitcnt vmcnt(63)
	v_add_f32_e32 v1, v1, v86
	global_load_dword v86, v4, s[0:1]
	s_add_u32 s0, s0, 0x20000
	s_addc_u32 s1, s1, 0
	s_waitcnt vmcnt(63)
	v_add_f32_e32 v1, v1, v87
	global_load_dword v87, v4, s[0:1]
	s_add_u32 s0, s0, 0x20000
	s_addc_u32 s1, s1, 0
	s_waitcnt vmcnt(63)
	v_add_f32_e32 v1, v1, v88
	global_load_dword v88, v4, s[0:1]
	s_add_u32 s0, s0, 0x20000
	s_addc_u32 s1, s1, 0
	s_waitcnt vmcnt(63)
	v_add_f32_e32 v1, v1, v89
	global_load_dword v89, v4, s[0:1]
	s_add_u32 s0, s0, 0x20000
	s_addc_u32 s1, s1, 0
	s_waitcnt vmcnt(63)
	v_add_f32_e32 v1, v1, v90
	global_load_dword v90, v4, s[0:1]
	s_add_u32 s0, s0, 0x20000
	s_addc_u32 s1, s1, 0
	s_waitcnt vmcnt(63)
	v_add_f32_e32 v1, v1, v91
	global_load_dword v91, v4, s[0:1]
	s_add_u32 s0, s0, 0x20000
	s_addc_u32 s1, s1, 0
	s_waitcnt vmcnt(63)
	v_add_f32_e32 v1, v1, v92
	global_load_dword v92, v4, s[0:1]
	s_add_u32 s0, s0, 0x20000
	s_addc_u32 s1, s1, 0
	s_waitcnt vmcnt(63)
	v_add_f32_e32 v1, v1, v93
	global_load_dword v93, v4, s[0:1]
	s_add_u32 s0, s0, 0x20000
	s_addc_u32 s1, s1, 0
	s_waitcnt vmcnt(63)
	v_add_f32_e32 v1, v1, v94
	global_load_dword v94, v4, s[0:1]
	s_add_u32 s0, s0, 0x20000
	s_addc_u32 s1, s1, 0
	s_waitcnt vmcnt(63)
	v_add_f32_e32 v1, v1, v95
	global_load_dword v95, v4, s[0:1]
	s_add_u32 s0, s0, 0x20000
	s_addc_u32 s1, s1, 0
	s_waitcnt vmcnt(63)
	v_add_f32_e32 v1, v1, v32
	s_waitcnt vmcnt(62)
	v_add_f32_e32 v1, v1, v33
	s_waitcnt vmcnt(61)
	v_add_f32_e32 v1, v1, v34
	s_waitcnt vmcnt(60)
	v_add_f32_e32 v1, v1, v35
	s_waitcnt vmcnt(59)
	v_add_f32_e32 v1, v1, v36
	s_waitcnt vmcnt(58)
	v_add_f32_e32 v1, v1, v37
	s_waitcnt vmcnt(57)
	v_add_f32_e32 v1, v1, v38
	s_waitcnt vmcnt(56)
	v_add_f32_e32 v1, v1, v39
	s_waitcnt vmcnt(55)
	v_add_f32_e32 v1, v1, v40
	s_waitcnt vmcnt(54)
	v_add_f32_e32 v1, v1, v41
	s_waitcnt vmcnt(53)
	v_add_f32_e32 v1, v1, v42
	s_waitcnt vmcnt(52)
	v_add_f32_e32 v1, v1, v43
	s_waitcnt vmcnt(51)
	v_add_f32_e32 v1, v1, v44
	s_waitcnt vmcnt(50)
	v_add_f32_e32 v1, v1, v45
	s_waitcnt vmcnt(49)
	v_add_f32_e32 v1, v1, v46
	s_waitcnt vmcnt(48)
	v_add_f32_e32 v1, v1, v47
	s_waitcnt vmcnt(47)
	v_add_f32_e32 v1, v1, v48
	s_waitcnt vmcnt(46)
	v_add_f32_e32 v1, v1, v49
	s_waitcnt vmcnt(45)
	v_add_f32_e32 v1, v1, v50
	s_waitcnt vmcnt(44)
	v_add_f32_e32 v1, v1, v51
	s_waitcnt vmcnt(43)
	v_add_f32_e32 v1, v1, v52
	s_waitcnt vmcnt(42)
	v_add_f32_e32 v1, v1, v53
	s_waitcnt vmcnt(41)
	v_add_f32_e32 v1, v1, v54
	s_waitcnt vmcnt(40)
	v_add_f32_e32 v1, v1, v55
	s_waitcnt vmcnt(39)
	v_add_f32_e32 v1, v1, v56
	s_waitcnt vmcnt(38)
	v_add_f32_e32 v1, v1, v57
	s_waitcnt vmcnt(37)
	v_add_f32_e32 v1, v1, v58
	s_waitcnt vmcnt(36)
	v_add_f32_e32 v1, v1, v59
	s_waitcnt vmcnt(35)
	v_add_f32_e32 v1, v1, v60
	s_waitcnt vmcnt(34)
	v_add_f32_e32 v1, v1, v61
	s_waitcnt vmcnt(33)
	v_add_f32_e32 v1, v1, v62
	s_waitcnt vmcnt(32)
	v_add_f32_e32 v1, v1, v63
	s_waitcnt vmcnt(31)
	v_add_f32_e32 v1, v1, v64
	s_waitcnt vmcnt(30)
	v_add_f32_e32 v1, v1, v65
	s_waitcnt vmcnt(29)
	v_add_f32_e32 v1, v1, v66
	s_waitcnt vmcnt(28)
	v_add_f32_e32 v1, v1, v67
	s_waitcnt vmcnt(27)
	v_add_f32_e32 v1, v1, v68
	s_waitcnt vmcnt(26)
	v_add_f32_e32 v1, v1, v69
	s_waitcnt vmcnt(25)
	v_add_f32_e32 v1, v1, v70
	s_waitcnt vmcnt(24)
	v_add_f32_e32 v1, v1, v71
	s_waitcnt vmcnt(23)
	v_add_f32_e32 v1, v1, v72
	s_waitcnt vmcnt(22)
	v_add_f32_e32 v1, v1, v73
	s_waitcnt vmcnt(21)
	v_add_f32_e32 v1, v1, v74
	s_waitcnt vmcnt(20)
	v_add_f32_e32 v1, v1, v75
	s_waitcnt vmcnt(19)
	v_add_f32_e32 v1, v1, v76
	s_waitcnt vmcnt(18)
	v_add_f32_e32 v1, v1, v77
	s_waitcnt vmcnt(17)
	v_add_f32_e32 v1, v1, v78
	s_waitcnt vmcnt(16)
	v_add_f32_e32 v1, v1, v79
	s_waitcnt vmcnt(15)
	v_add_f32_e32 v1, v1, v80
	s_waitcnt vmcnt(14)
	v_add_f32_e32 v1, v1, v81
	s_waitcnt vmcnt(13)
	v_add_f32_e32 v1, v1, v82
	s_waitcnt vmcnt(12)
	v_add_f32_e32 v1, v1, v83
	s_waitcnt vmcnt(11)
	v_add_f32_e32 v1, v1, v84
	s_waitcnt vmcnt(10)
	v_add_f32_e32 v1, v1, v85
	s_waitcnt vmcnt(9)
	v_add_f32_e32 v1, v1, v86
	s_waitcnt vmcnt(8)
	v_add_f32_e32 v1, v1, v87
	s_waitcnt vmcnt(7)
	v_add_f32_e32 v1, v1, v88
	s_waitcnt vmcnt(6)
	v_add_f32_e32 v1, v1, v89
	s_waitcnt vmcnt(5)
	v_add_f32_e32 v1, v1, v90
	s_waitcnt vmcnt(4)
	v_add_f32_e32 v1, v1, v91
	s_waitcnt vmcnt(3)
	v_add_f32_e32 v1, v1, v92
	s_waitcnt vmcnt(2)
	v_add_f32_e32 v1, v1, v93
	s_waitcnt vmcnt(1)
	v_add_f32_e32 v1, v1, v94
	s_waitcnt vmcnt(0)
	v_add_f32_e32 v1, v1, v95
	v_max_f32_e32 v1, v1, v1
	s_movk_i32 s0, 0x280
	v_max_f32_e32 v1, 0, v1
	v_lshlrev_b32_e32 v2, 2, v0
	v_cmp_gt_u32_e32 vcc, s0, v0
	ds_write_b32 v2, v1
	s_waitcnt lgkmcnt(0)
	s_barrier
	s_and_saveexec_b64 s[0:1], vcc
	s_cbranch_execz .LBB6_7
	v_and_b32_e32 v1, 63, v0
	v_lshrrev_b32_e32 v12, 6, v0
	v_mbcnt_lo_u32_b32 v0, -1, 0
	v_mbcnt_hi_u32_b32 v0, -1, v0
	v_bitop3_b32 v3, v0, 63, v0 bitop3:0xc
	v_bitop3_b32 v4, v0, 32, 63 bitop3:8
	v_cmp_gt_u32_e64 s[0:1], 16, v3
	v_add_lshl_u32 v13, v4, v0, 2
	v_and_b32_e32 v2, 63, v0
	v_cndmask_b32_e64 v4, 16, 0, s[0:1]
	v_cmp_gt_u32_e64 s[0:1], 8, v3
	v_add_lshl_u32 v14, v4, v0, 2
	v_lshlrev_b32_e32 v19, 2, v1
	v_cndmask_b32_e64 v4, 8, 0, s[0:1]
	v_cmp_gt_u32_e64 s[0:1], 4, v3
	v_add_lshl_u32 v15, v4, v0, 2
	v_cmp_eq_u32_e32 vcc, 0, v1
	v_cndmask_b32_e64 v4, 4, 0, s[0:1]
	v_cmp_gt_u32_e64 s[0:1], 2, v3
	v_add_lshl_u32 v16, v4, v0, 2
	v_lshlrev_b32_e32 v8, 2, v12
	v_cndmask_b32_e64 v3, 2, 0, s[0:1]
	v_cmp_ne_u32_e64 s[0:1], 63, v2
	v_add_lshl_u32 v17, v3, v0, 2
	v_mov_b32_e32 v9, 0
	v_addc_co_u32_e64 v0, s[0:1], 0, v0, s[0:1]
	v_lshlrev_b32_e32 v18, 2, v0
	ds_read2st64_b32 v[0:1], v19 offset0:2 offset1:3
	ds_read2st64_b32 v[2:3], v19 offset0:4 offset1:5
	ds_read2st64_b32 v[4:5], v19 offset0:6 offset1:7
	ds_read2st64_b32 v[6:7], v19 offset1:1
	s_mul_i32 s4, s2, 10
	v_lshl_add_u64 v[10:11], s[10:11], 0, v[8:9]
	v_lshl_or_b32 v8, v12, 11, v19
	s_mov_b64 s[2:3], 0
	s_branch .LBB6_5

	.amdhsa_kernel _Z5k_fc2PKfS0_S0_S0_Pf
		.amdhsa_group_segment_fixed_size 2048
		.amdhsa_private_segment_fixed_size 0
		.amdhsa_kernarg_size 40
		.amdhsa_user_sgpr_count 2
		.amdhsa_user_sgpr_dispatch_ptr 0
		.amdhsa_user_sgpr_queue_ptr 0
		.amdhsa_user_sgpr_kernarg_segment_ptr 1
		.amdhsa_user_sgpr_dispatch_id 0
		.amdhsa_user_sgpr_kernarg_preload_length 0
		.amdhsa_user_sgpr_kernarg_preload_offset 0
		.amdhsa_user_sgpr_private_segment_size 0
		.amdhsa_uses_dynamic_stack 0
		.amdhsa_enable_private_segment 0
		.amdhsa_system_sgpr_workgroup_id_x 1
		.amdhsa_system_sgpr_workgroup_id_y 0
		.amdhsa_system_sgpr_workgroup_id_z 0
		.amdhsa_system_sgpr_workgroup_info 0
		.amdhsa_system_vgpr_workitem_id 0
		.amdhsa_next_free_vgpr 96
		.amdhsa_next_free_sgpr 12
		.amdhsa_accum_offset 96
		.amdhsa_reserve_vcc 1
		.amdhsa_float_round_mode_32 0
		.amdhsa_float_round_mode_16_64 0
		.amdhsa_float_denorm_mode_32 3
		.amdhsa_float_denorm_mode_16_64 3
		.amdhsa_dx10_clamp 1
		.amdhsa_ieee_mode 1
		.amdhsa_fp16_overflow 0
		.amdhsa_tg_split 0
		.amdhsa_exception_fp_ieee_invalid_op 0
		.amdhsa_exception_fp_denorm_src 0
		.amdhsa_exception_fp_ieee_div_zero 0
		.amdhsa_exception_fp_ieee_overflow 0
		.amdhsa_exception_fp_ieee_underflow 0
		.amdhsa_exception_fp_ieee_inexact 0
		.amdhsa_exception_int_div_zero 0
	.end_amdhsa_kernel

amdhsa.kernels:
  - .agpr_count:     0
    .args:
      - .actual_access:  read_only
        .address_space:  global
        .offset:         0
        .size:           8
        .value_kind:     global_buffer
      - .actual_access:  read_only
        .address_space:  global
        .offset:         8
        .size:           8
        .value_kind:     global_buffer
      - .actual_access:  write_only
        .address_space:  global
        .offset:         16
        .size:           8
        .value_kind:     global_buffer
      - .actual_access:  write_only
        .address_space:  global
        .offset:         24
        .size:           8
        .value_kind:     global_buffer
      - .actual_access:  write_only
        .address_space:  global
        .offset:         32
        .size:           8
        .value_kind:     global_buffer
      - .actual_access:  read_only
        .address_space:  global
        .offset:         40
        .size:           8
        .value_kind:     global_buffer
    .group_segment_fixed_size: 1024
    .kernarg_segment_align: 8
    .kernarg_segment_size: 48
    .language:       OpenCL C
    .language_version:
      - 2
      - 0
    .max_flat_workgroup_size: 1024
    .name:           _Z7k_sort2PKiPKfPiS3_S3_Pf
    .private_segment_fixed_size: 0
    .sgpr_count:     18
    .sgpr_spill_count: 0
    .symbol:         _Z7k_sort2PKiPKfPiS3_S3_Pf.kd
    .uniform_work_group_size: 1
    .uses_dynamic_stack: false
    .vgpr_count:     21
    .vgpr_spill_count: 0
    .wavefront_size: 64
  - .agpr_count:     0
    .args:
      - .actual_access:  read_only
        .address_space:  global
        .offset:         0
        .size:           8
        .value_kind:     global_buffer
      - .actual_access:  read_only
        .address_space:  global
        .offset:         8
        .size:           8
        .value_kind:     global_buffer
      - .actual_access:  read_only
        .address_space:  global
        .offset:         16
        .size:           8
        .value_kind:     global_buffer
      - .actual_access:  read_only
        .address_space:  global
        .offset:         24
        .size:           8
        .value_kind:     global_buffer
      - .actual_access:  read_only
        .address_space:  global
        .offset:         32
        .size:           8
        .value_kind:     global_buffer
      - .actual_access:  read_only
        .address_space:  global
        .offset:         40
        .size:           8
        .value_kind:     global_buffer
      - .address_space:  global
        .offset:         48
        .size:           8
        .value_kind:     global_buffer
      - .address_space:  global
        .offset:         56
        .size:           8
        .value_kind:     global_buffer
      - .offset:         64
        .size:           4
        .value_kind:     by_value
      - .offset:         68
        .size:           4
        .value_kind:     by_value
    .group_segment_fixed_size: 0
    .kernarg_segment_align: 8
    .kernarg_segment_size: 72
    .language:       OpenCL C
    .language_version:
      - 2
      - 0
    .max_flat_workgroup_size: 512
    .name:           _Z7k_spmm1PKiS0_PKfPK15HIP_vector_typeIjLj2EES0_S2_S2_Pfff
    .private_segment_fixed_size: 0
    .sgpr_count:     26
    .sgpr_spill_count: 0
    .symbol:         _Z7k_spmm1PKiS0_PKfPK15HIP_vector_typeIjLj2EES0_S2_S2_Pfff.kd
    .uniform_work_group_size: 1
    .uses_dynamic_stack: false
    .vgpr_count:     41
    .vgpr_spill_count: 0
    .wavefront_size: 64
  - .agpr_count:     0
    .args:
      - .address_space:  global
        .offset:         0
        .size:           8
        .value_kind:     global_buffer
      - .actual_access:  read_only
        .address_space:  global
        .offset:         8
        .size:           8
        .value_kind:     global_buffer
      - .actual_access:  read_only
        .address_space:  global
        .offset:         16
        .size:           8
        .value_kind:     global_buffer
      - .actual_access:  write_only
        .address_space:  global
        .offset:         24
        .size:           8
        .value_kind:     global_buffer
    .group_segment_fixed_size: 32768
    .kernarg_segment_align: 8
    .kernarg_segment_size: 32
    .language:       OpenCL C
    .language_version:
      - 2
      - 0
    .max_flat_workgroup_size: 512
    .name:           _Z7k_conv1PKfS0_S0_Pf
    .private_segment_fixed_size: 0
    .sgpr_count:     20
    .sgpr_spill_count: 0
    .symbol:         _Z7k_conv1PKfS0_S0_Pf.kd
    .uniform_work_group_size: 1
    .uses_dynamic_stack: false
    .vgpr_count:     107
    .vgpr_spill_count: 0
    .wavefront_size: 64
  - .agpr_count:     0
    .args:
      - .actual_access:  read_only
        .address_space:  global
        .offset:         0
        .size:           8
        .value_kind:     global_buffer
      - .actual_access:  read_only
        .address_space:  global
        .offset:         8
        .size:           8
        .value_kind:     global_buffer
      - .actual_access:  read_only
        .address_space:  global
        .offset:         16
        .size:           8
        .value_kind:     global_buffer
      - .address_space:  global
        .offset:         24
        .size:           8
        .value_kind:     global_buffer
      - .actual_access:  read_only
        .address_space:  global
        .offset:         32
        .size:           8
        .value_kind:     global_buffer
      - .actual_access:  read_only
        .address_space:  global
        .offset:         40
        .size:           8
        .value_kind:     global_buffer
      - .actual_access:  write_only
        .address_space:  global
        .offset:         48
        .size:           8
        .value_kind:     global_buffer
      - .actual_access:  write_only
        .address_space:  global
        .offset:         56
        .size:           8
        .value_kind:     global_buffer
      - .actual_access:  write_only
        .address_space:  global
        .offset:         64
        .size:           8
        .value_kind:     global_buffer
    .group_segment_fixed_size: 139392
    .kernarg_segment_align: 8
    .kernarg_segment_size: 72
    .language:       OpenCL C
    .language_version:
      - 2
      - 0
    .max_flat_workgroup_size: 512
    .name:           _Z6k_rec2PKiS0_S0_PK15HIP_vector_typeIjLj4EEPKfS6_PS2_PS1_IjLj2EEPf
    .private_segment_fixed_size: 0
    .sgpr_count:     75
    .sgpr_spill_count: 0
    .symbol:         _Z6k_rec2PKiS0_S0_PK15HIP_vector_typeIjLj4EEPKfS6_PS2_PS1_IjLj2EEPf.kd
    .uniform_work_group_size: 1
    .uses_dynamic_stack: false
    .vgpr_count:     246
    .vgpr_spill_count: 0
    .wavefront_size: 64
  - .agpr_count:     0
    .args:
      - .address_space:  global
        .offset:         0
        .size:           8
        .value_kind:     global_buffer
      - .address_space:  global
        .offset:         8
        .size:           8
        .value_kind:     global_buffer
      - .actual_access:  read_only
        .address_space:  global
        .offset:         16
        .size:           8
        .value_kind:     global_buffer
      - .actual_access:  read_only
        .address_space:  global
        .offset:         24
        .size:           8
        .value_kind:     global_buffer
      - .actual_access:  read_only
        .address_space:  global
        .offset:         32
        .size:           8
        .value_kind:     global_buffer
      - .actual_access:  read_only
        .address_space:  global
        .offset:         40
        .size:           8
        .value_kind:     global_buffer
      - .actual_access:  write_only
        .address_space:  global
        .offset:         48
        .size:           8
        .value_kind:     global_buffer
      - .actual_access:  write_only
        .address_space:  global
        .offset:         56
        .size:           8
        .value_kind:     global_buffer
    .group_segment_fixed_size: 127376
    .kernarg_segment_align: 8
    .kernarg_segment_size: 64
    .language:       OpenCL C
    .language_version:
      - 2
      - 0
    .max_flat_workgroup_size: 1024
    .name:           _Z7k_gemm2PK15HIP_vector_typeIjLj4EEPKS_IjLj2EEPKfS2_S2_S7_PtS8_
    .private_segment_fixed_size: 0
    .sgpr_count:     26
    .sgpr_spill_count: 0
    .symbol:         _Z7k_gemm2PK15HIP_vector_typeIjLj4EEPKS_IjLj2EEPKfS2_S2_S7_PtS8_.kd
    .uniform_work_group_size: 1
    .uses_dynamic_stack: false
    .vgpr_count:     115
    .vgpr_spill_count: 0
    .wavefront_size: 64
  - .agpr_count:     32
    .args:
      - .address_space:  global
        .offset:         0
        .size:           8
        .value_kind:     global_buffer
      - .address_space:  global
        .offset:         8
        .size:           8
        .value_kind:     global_buffer
      - .address_space:  global
        .offset:         16
        .size:           8
        .value_kind:     global_buffer
      - .actual_access:  write_only
        .address_space:  global
        .offset:         24
        .size:           8
        .value_kind:     global_buffer
    .group_segment_fixed_size: 65536
    .kernarg_segment_align: 8
    .kernarg_segment_size: 32
    .language:       OpenCL C
    .language_version:
      - 2
      - 0
    .max_flat_workgroup_size: 256
    .name:           _Z5k_fc1PKtS0_PKfPf
    .private_segment_fixed_size: 0
    .sgpr_count:     49
    .sgpr_spill_count: 0
    .symbol:         _Z5k_fc1PKtS0_PKfPf.kd
    .uniform_work_group_size: 1
    .uses_dynamic_stack: false
    .vgpr_count:     172
    .vgpr_spill_count: 0
    .wavefront_size: 64
  - .agpr_count:     0
    .args:
      - .actual_access:  read_only
        .address_space:  global
        .offset:         0
        .size:           8
        .value_kind:     global_buffer
      - .actual_access:  read_only
        .address_space:  global
        .offset:         8
        .size:           8
        .value_kind:     global_buffer
      - .actual_access:  read_only
        .address_space:  global
        .offset:         16
        .size:           8
        .value_kind:     global_buffer
      - .actual_access:  read_only
        .address_space:  global
        .offset:         24
        .size:           8
        .value_kind:     global_buffer
      - .actual_access:  write_only
        .address_space:  global
        .offset:         32
        .size:           8
        .value_kind:     global_buffer
    .group_segment_fixed_size: 2048
    .kernarg_segment_align: 8
    .kernarg_segment_size: 40
    .language:       OpenCL C
    .language_version:
      - 2
      - 0
    .max_flat_workgroup_size: 512
    .name:           _Z5k_fc2PKfS0_S0_S0_Pf
    .private_segment_fixed_size: 0
    .sgpr_count:     18
    .sgpr_spill_count: 0
    .symbol:         _Z5k_fc2PKfS0_S0_S0_Pf.kd
    .uniform_work_group_size: 1
    .uses_dynamic_stack: false
    .vgpr_count:     96
    .vgpr_spill_count: 0
    .wavefront_size: 64
  - .agpr_count:     0
    .args:
      - .actual_access:  read_only
        .address_space:  global
        .offset:         0
        .size:           8
        .value_kind:     global_buffer
      - .actual_access:  read_only
        .address_space:  global
        .offset:         8
        .size:           8
        .value_kind:     global_buffer
      - .actual_access:  read_only
        .address_space:  global
        .offset:         16
        .size:           8
        .value_kind:     global_buffer
      - .actual_access:  read_only
        .address_space:  global
        .offset:         24
        .size:           8
        .value_kind:     global_buffer
      - .actual_access:  write_only
        .address_space:  global
        .offset:         32
        .size:           8
        .value_kind:     global_buffer
      - .actual_access:  write_only
        .address_space:  global
        .offset:         40
        .size:           8
        .value_kind:     global_buffer
      - .actual_access:  write_only
        .address_space:  global
        .offset:         48
        .size:           8
        .value_kind:     global_buffer
      - .actual_access:  write_only
        .address_space:  global
        .offset:         56
        .size:           8
        .value_kind:     global_buffer
      - .actual_access:  write_only
        .address_space:  global
        .offset:         64
        .size:           8
        .value_kind:     global_buffer
    .group_segment_fixed_size: 16640
    .kernarg_segment_align: 8
    .kernarg_segment_size: 72
    .language:       OpenCL C
    .language_version:
      - 2
      - 0
    .max_flat_workgroup_size: 256
    .name:           _Z7k_prepAPKiS0_PKfS2_PiS3_PtS4_Pf
    .private_segment_fixed_size: 0
    .sgpr_count:     20
    .sgpr_spill_count: 0
    .symbol:         _Z7k_prepAPKiS0_PKfS2_PiS3_PtS4_Pf.kd
    .uniform_work_group_size: 1
    .uses_dynamic_stack: false
    .vgpr_count:     24
    .vgpr_spill_count: 0
    .wavefront_size: 64
  - .agpr_count:     0
    .args:
      - .actual_access:  read_only
        .address_space:  global
        .offset:         0
        .size:           8
        .value_kind:     global_buffer
      - .actual_access:  read_only
        .address_space:  global
        .offset:         8
        .size:           8
        .value_kind:     global_buffer
      - .actual_access:  read_only
        .address_space:  global
        .offset:         16
        .size:           8
        .value_kind:     global_buffer
      - .actual_access:  write_only
        .address_space:  global
        .offset:         24
        .size:           8
        .value_kind:     global_buffer
      - .actual_access:  write_only
        .address_space:  global
        .offset:         32
        .size:           8
        .value_kind:     global_buffer
      - .actual_access:  read_only
        .address_space:  global
        .offset:         40
        .size:           8
        .value_kind:     global_buffer
      - .actual_access:  read_only
        .address_space:  global
        .offset:         48
        .size:           8
        .value_kind:     global_buffer
      - .actual_access:  read_only
        .address_space:  global
        .offset:         56
        .size:           8
        .value_kind:     global_buffer
      - .actual_access:  read_only
        .address_space:  global
        .offset:         64
        .size:           8
        .value_kind:     global_buffer
      - .actual_access:  read_only
        .address_space:  global
        .offset:         72
        .size:           8
        .value_kind:     global_buffer
      - .actual_access:  read_only
        .address_space:  global
        .offset:         80
        .size:           8
        .value_kind:     global_buffer
      - .actual_access:  read_only
        .address_space:  global
        .offset:         88
        .size:           8
        .value_kind:     global_buffer
      - .actual_access:  write_only
        .address_space:  global
        .offset:         96
        .size:           8
        .value_kind:     global_buffer
    .group_segment_fixed_size: 0
    .kernarg_segment_align: 8
    .kernarg_segment_size: 104
    .language:       OpenCL C
    .language_version:
      - 2
      - 0
    .max_flat_workgroup_size: 256
    .name:           _Z7k_prepBPKiS0_PKfP15HIP_vector_typeIjLj2EEPiS0_S0_S2_S0_S0_S0_S2_Pj
    .private_segment_fixed_size: 0
    .sgpr_count:     21
    .sgpr_spill_count: 0
    .symbol:         _Z7k_prepBPKiS0_PKfP15HIP_vector_typeIjLj2EEPiS0_S0_S2_S0_S0_S0_S2_Pj.kd
    .uniform_work_group_size: 1
    .uses_dynamic_stack: false
    .vgpr_count:     14
    .vgpr_spill_count: 0
    .wavefront_size: 64
